# speedup vs baseline: 1.0172x; 1.0172x over previous
_Z13prep_w_kernelPKfS0_S0_PDv8_DF16_:
	s_load_dwordx8 s[4:11], s[0:1], 0x0
	s_lshl_b32 s2, s2, 6
	v_add_u32_e32 v0, s2, v0
	s_movk_i32 s2, 0x6000
	v_cmp_gt_i32_e32 vcc, s2, v0
	s_and_saveexec_b64 s[2:3], vcc
	s_cbranch_execz .LBB0_2
	v_ashrrev_i32_e32 v1, 6, v0
	s_mov_b32 s0, 0x55555556
	v_mul_hi_i32 v2, v1, s0
	v_lshrrev_b32_e32 v3, 31, v2
	v_add_u32_e32 v4, v2, v3
	v_lshl_add_u32 v2, v4, 1, v4
	s_mov_b32 s0, 0x2aaaaaab
	v_sub_u32_e32 v2, v1, v2
	v_mul_hi_i32 v1, v1, s0
	v_lshrrev_b32_e32 v3, 31, v1
	v_lshrrev_b32_e32 v1, 4, v1
	v_add_u32_e32 v1, v1, v3
	s_waitcnt lgkmcnt(0)
	v_mov_b32_e32 v3, s8
	v_mov_b32_e32 v5, s6
	v_cmp_eq_u32_e32 vcc, 1, v2
	v_mov_b32_e32 v6, s7
	v_lshlrev_b32_e32 v4, 5, v4
	v_cndmask_b32_e32 v5, v3, v5, vcc
	v_mov_b32_e32 v3, s9
	v_cndmask_b32_e32 v3, v3, v6, vcc
	v_cmp_eq_u32_e32 vcc, 0, v2
	v_mov_b32_e32 v2, s5
	v_and_b32_e32 v4, 0x3e0, v4
	v_cndmask_b32_e32 v3, v3, v2, vcc
	v_mov_b32_e32 v2, s4
	v_cndmask_b32_e32 v2, v5, v2, vcc
	v_lshrrev_b32_e32 v5, 1, v0
	v_and_or_b32 v5, v5, 24, v4
	v_and_b32_e32 v4, 15, v0
	v_lshl_or_b32 v4, v1, 4, v4
	v_lshlrev_b32_e32 v8, 6, v5
	v_add_u32_e32 v10, v4, v8
	v_ashrrev_i32_e32 v11, 31, v10
	v_ashrrev_i32_e32 v5, 31, v4
	v_mov_b32_e32 v9, 0
	v_mov_b32_e32 v6, 0x42800000
	v_mov_b32_e32 v7, 0x4138aa3b
	v_lshl_add_u64 v[10:11], v[10:11], 2, v[2:3]
	v_lshl_add_u64 v[4:5], v[4:5], 0, v[8:9]
	v_cndmask_b32_e32 v6, v6, v7, vcc
	v_lshl_add_u64 v[2:3], v[4:5], 2, v[2:3]
	global_load_dword v7, v[10:11], off
	global_load_dword v4, v[2:3], off offset:256
	global_load_dword v5, v[2:3], off offset:512
	global_load_dword v8, v[2:3], off offset:768
	global_load_dword v9, v[2:3], off offset:1024
	global_load_dword v12, v[2:3], off offset:1280
	global_load_dword v13, v[2:3], off offset:1536
	global_load_dword v14, v[2:3], off offset:1792
	v_ashrrev_i32_e32 v1, 31, v0
	v_lshl_add_u64 v[0:1], v[0:1], 4, s[10:11]
	s_waitcnt vmcnt(7)
	v_fma_mixlo_f16 v7, v6, v7, 0
	s_waitcnt vmcnt(5)
	v_pk_mul_f32 v[2:3], v[6:7], v[4:5] op_sel_hi:[0,1]
	v_cvt_pk_f16_f32 v3, v2, v3
	s_waitcnt vmcnt(3)
	v_pk_mul_f32 v[4:5], v[6:7], v[8:9] op_sel_hi:[0,1]
	v_cvt_pk_f16_f32 v4, v4, v5
	s_waitcnt vmcnt(1)
	v_pk_mul_f32 v[8:9], v[6:7], v[12:13] op_sel_hi:[0,1]
	v_cvt_pk_f16_f32 v5, v8, v9
	v_pack_b32_f16 v2, v7, v3
	v_alignbit_b32 v3, v4, v3, 16
	v_alignbit_b32 v4, v5, v4, 16
	v_lshrrev_b32_e32 v5, 16, v5
	s_waitcnt vmcnt(0)
	v_fma_mixhi_f16 v5, v6, v14, 0
	global_store_dwordx4 v[0:1], v[2:5], off sc1
